# A1 epilogue: hoist redundant per-row-group SWQ/SA scale reloads (load once into spare VGPRs), removing store->load latency chain
# speedup vs baseline: 1.0032x; 1.0032x over previous
.LBB0_245:
	v_cvt_f32_i32_e32 v137, v127
	v_cvt_f32_i32_e32 v136, v126
	v_cvt_f32_i32_e32 v139, v125
	v_cvt_f32_i32_e32 v138, v124
	v_cvt_f32_i32_e32 v141, v123
	v_cvt_f32_i32_e32 v140, v122
	v_cvt_f32_i32_e32 v143, v121
	v_cvt_f32_i32_e32 v142, v120
	v_cvt_f32_i32_e32 v119, v119
	v_cvt_f32_i32_e32 v118, v118
	v_cvt_f32_i32_e32 v117, v117
	v_cvt_f32_i32_e32 v116, v116
	v_cvt_f32_i32_e32 v115, v115
	v_cvt_f32_i32_e32 v114, v114
	v_cvt_f32_i32_e32 v113, v113
	v_cvt_f32_i32_e32 v112, v112
	v_cvt_f32_i32_e32 v111, v111
	v_cvt_f32_i32_e32 v110, v110
	v_cvt_f32_i32_e32 v109, v109
	v_cvt_f32_i32_e32 v108, v108
	v_cvt_f32_i32_e32 v107, v107
	v_cvt_f32_i32_e32 v106, v106
	v_cvt_f32_i32_e32 v105, v105
	v_cvt_f32_i32_e32 v104, v104
	v_cvt_f32_i32_e32 v103, v103
	v_cvt_f32_i32_e32 v102, v102
	v_cvt_f32_i32_e32 v101, v101
	v_cvt_f32_i32_e32 v100, v100
	v_cvt_f32_i32_e32 v99, v99
	v_cvt_f32_i32_e32 v98, v98
	v_cvt_f32_i32_e32 v97, v97
	v_cvt_f32_i32_e32 v96, v96
	v_cvt_f32_i32_e32 v123, v95
	v_cvt_f32_i32_e32 v122, v94
	v_cvt_f32_i32_e32 v125, v93
	v_cvt_f32_i32_e32 v124, v92
	v_cvt_f32_i32_e32 v127, v91
	v_cvt_f32_i32_e32 v126, v90
	v_cvt_f32_i32_e32 v133, v89
	v_cvt_f32_i32_e32 v132, v88
	v_cvt_f32_i32_e32 v89, v87
	v_cvt_f32_i32_e32 v88, v86
	v_cvt_f32_i32_e32 v91, v85
	v_cvt_f32_i32_e32 v90, v84
	v_cvt_f32_i32_e32 v93, v83
	v_cvt_f32_i32_e32 v92, v82
	v_cvt_f32_i32_e32 v95, v81
	v_cvt_f32_i32_e32 v94, v80
	v_cvt_f32_i32_e32 v79, v79
	v_cvt_f32_i32_e32 v78, v78
	v_cvt_f32_i32_e32 v81, v77
	v_cvt_f32_i32_e32 v80, v76
	v_cvt_f32_i32_e32 v83, v75
	v_cvt_f32_i32_e32 v82, v74
	v_cvt_f32_i32_e32 v85, v73
	v_cvt_f32_i32_e32 v84, v72
	v_cvt_f32_i32_e32 v71, v71
	v_cvt_f32_i32_e32 v70, v70
	v_cvt_f32_i32_e32 v69, v69
	v_cvt_f32_i32_e32 v68, v68
	v_cvt_f32_i32_e32 v73, v67
	v_cvt_f32_i32_e32 v72, v66
	v_cvt_f32_i32_e32 v75, v65
	v_cvt_f32_i32_e32 v74, v64
	v_cvt_f32_i32_e32 v63, v63
	v_cvt_f32_i32_e32 v62, v62
	v_cvt_f32_i32_e32 v61, v61
	v_cvt_f32_i32_e32 v60, v60
	v_cvt_f32_i32_e32 v59, v59
	v_cvt_f32_i32_e32 v58, v58
	v_cvt_f32_i32_e32 v65, v57
	v_cvt_f32_i32_e32 v64, v56
	v_cvt_f32_i32_e32 v55, v55
	v_cvt_f32_i32_e32 v54, v54
	v_cvt_f32_i32_e32 v53, v53
	v_cvt_f32_i32_e32 v52, v52
	v_cvt_f32_i32_e32 v51, v51
	v_cvt_f32_i32_e32 v50, v50
	v_cvt_f32_i32_e32 v49, v49
	v_cvt_f32_i32_e32 v48, v48
	v_cvt_f32_i32_e32 v47, v47
	v_cvt_f32_i32_e32 v46, v46
	v_cvt_f32_i32_e32 v45, v45
	v_cvt_f32_i32_e32 v44, v44
	v_cvt_f32_i32_e32 v43, v43
	v_cvt_f32_i32_e32 v42, v42
	v_cvt_f32_i32_e32 v41, v41
	v_cvt_f32_i32_e32 v40, v40
	v_cvt_f32_i32_e32 v39, v39
	v_cvt_f32_i32_e32 v38, v38
	v_cvt_f32_i32_e32 v37, v37
	v_cvt_f32_i32_e32 v36, v36
	v_cvt_f32_i32_e32 v35, v35
	v_cvt_f32_i32_e32 v34, v34
	v_cvt_f32_i32_e32 v33, v33
	v_cvt_f32_i32_e32 v32, v32
	v_cvt_f32_i32_e32 v31, v31
	v_cvt_f32_i32_e32 v30, v30
	v_cvt_f32_i32_e32 v29, v29
	v_cvt_f32_i32_e32 v28, v28
	v_cvt_f32_i32_e32 v27, v27
	v_cvt_f32_i32_e32 v26, v26
	v_cvt_f32_i32_e32 v25, v25
	v_cvt_f32_i32_e32 v24, v24
	v_cvt_f32_i32_e32 v23, v23
	v_cvt_f32_i32_e32 v22, v22
	v_cvt_f32_i32_e32 v21, v21
	v_cvt_f32_i32_e32 v20, v20
	v_cvt_f32_i32_e32 v19, v19
	v_cvt_f32_i32_e32 v18, v18
	v_cvt_f32_i32_e32 v17, v17
	v_cvt_f32_i32_e32 v16, v16
	v_cvt_f32_i32_e32 v15, v15
	v_cvt_f32_i32_e32 v14, v14
	v_cvt_f32_i32_e32 v13, v13
	v_cvt_f32_i32_e32 v12, v12
	v_cvt_f32_i32_e32 v11, v11
	v_cvt_f32_i32_e32 v10, v10
	v_cvt_f32_i32_e32 v9, v9
	v_cvt_f32_i32_e32 v8, v8
	v_cvt_f32_i32_e32 v7, v7
	v_cvt_f32_i32_e32 v6, v6
	v_cvt_f32_i32_e32 v5, v5
	v_cvt_f32_i32_e32 v4, v4
	v_cvt_f32_i32_e32 v3, v3
	v_cvt_f32_i32_e32 v2, v2
	v_cvt_f32_i32_e32 v1, v1
	v_cvt_f32_i32_e32 v0, v0
	v_readlane_b32 s2, v253, 24
	s_cmp_gt_i32 s10, 31
	s_mov_b64 s[0:1], -1
	v_readlane_b32 s3, v253, 25
	s_cbranch_scc0 .LBB0_311
	v_lshl_add_u32 v76, s10, 8, v185
	v_ashrrev_i32_e32 v77, 31, v76
	v_lshl_or_b32 v66, s11, 8, v128
	v_readlane_b32 s0, v253, 26
	v_lshl_add_u64 v[56:57], v[76:77], 2, s[16:17]
	v_ashrrev_i32_e32 v67, 31, v66
	v_readlane_b32 s1, v253, 27
	global_load_dword v154, v[56:57], off
	global_load_dword v152, v[56:57], off offset:64
	global_load_dword v150, v[56:57], off offset:128
	global_load_dword v148, v[56:57], off offset:192
	global_load_dword v146, v[56:57], off offset:512
	global_load_dword v144, v[56:57], off offset:576
	global_load_dword v134, v[56:57], off offset:640
	s_nop 0
	global_load_dword v56, v[56:57], off offset:704
	v_lshl_add_u64 v[86:87], v[66:67], 2, s[0:1]
	global_load_dwordx4 v[228:231], v[86:87], off
	global_load_dwordx4 v[232:235], v[86:87], off offset:16
	v_lshlrev_b64 v[120:121], 14, v[76:77]
	v_lshl_add_u64 v[120:121], s[96:97], 0, v[120:121]
	v_lshl_add_u64 v[156:157], v[66:67], 1, v[120:121]
	s_mov_b64 s[0:1], -1
	s_and_b64 vcc, exec, s[2:3]
	s_waitcnt vmcnt(9)
	v_pk_mul_f32 v[162:163], v[154:155], v[138:139] op_sel_hi:[0,1]
	v_pk_mul_f32 v[120:121], v[154:155], v[136:137] op_sel_hi:[0,1]
	v_pk_mul_f32 v[178:179], v[154:155], v[140:141] op_sel_hi:[0,1]
	v_pk_mul_f32 v[180:181], v[154:155], v[142:143] op_sel_hi:[0,1]
	s_waitcnt vmcnt(1)
	v_pk_mul_f32 v[120:121], v[120:121], v[230:231]
	v_pk_mul_f32 v[164:165], v[162:163], v[228:229]
	s_waitcnt vmcnt(0)
	v_pk_mul_f32 v[162:163], v[180:181], v[232:233]
	v_pk_mul_f32 v[160:161], v[178:179], v[234:235]
	s_cbranch_vccz .LBB0_248
	v_cvt_pk_bf16_f32 v174, v164, v165
	v_cvt_pk_bf16_f32 v175, v120, v121
	v_cvt_pk_bf16_f32 v176, v162, v163
	v_cvt_pk_bf16_f32 v177, v160, v161
	global_store_dwordx4 v[156:157], v[174:177], off
	s_mov_b64 s[0:1], 0

.LBB0_250:
	v_or_b32_e32 v120, 0x80, v66
	v_readlane_b32 s0, v253, 26
	v_ashrrev_i32_e32 v121, 31, v120
	v_readlane_b32 s1, v253, 27
	v_mov_b32_e32 v155, v154
	v_mov_b32_e32 v164, v154
	v_lshl_add_u64 v[120:121], v[120:121], 2, s[0:1]
	global_load_dwordx4 v[236:239], v[120:121], off
	global_load_dwordx4 v[240:243], v[120:121], off offset:16
	v_mov_b32_e32 v165, v154
	v_pk_mul_f32 v[178:179], v[164:165], v[122:123]
	v_pk_mul_f32 v[180:181], v[154:155], v[124:125]
	v_pk_mul_f32 v[208:209], v[164:165], v[126:127]
	v_pk_mul_f32 v[210:211], v[154:155], v[132:133]
	s_mov_b64 s[0:1], -1
	s_and_b64 vcc, exec, s[2:3]
	s_waitcnt vmcnt(1)
	v_pk_mul_f32 v[154:155], v[178:179], v[238:239]
	v_pk_mul_f32 v[164:165], v[180:181], v[236:237]
	s_waitcnt vmcnt(0)
	v_pk_mul_f32 v[160:161], v[208:209], v[242:243]
	v_pk_mul_f32 v[162:163], v[210:211], v[240:241]
	s_cbranch_vccz .LBB0_252
	v_cvt_pk_bf16_f32 v174, v164, v165
	v_cvt_pk_bf16_f32 v175, v154, v155
	v_cvt_pk_bf16_f32 v176, v162, v163
	v_cvt_pk_bf16_f32 v177, v160, v161
	global_store_dwordx4 v[156:157], v[174:177], off offset:256
	s_mov_b64 s[0:1], 0

.LBB0_254:
	s_nop 0
	s_nop 0
	v_or_b32_e32 v156, 16, v76
	v_ashrrev_i32_e32 v157, 31, v156
	v_lshlrev_b64 v[154:155], 14, v[156:157]
	v_pk_mul_f32 v[158:159], v[152:153], v[118:119] op_sel_hi:[0,1]
	v_pk_mul_f32 v[164:165], v[152:153], v[116:117] op_sel_hi:[0,1]
	v_pk_mul_f32 v[178:179], v[152:153], v[114:115] op_sel_hi:[0,1]
	v_pk_mul_f32 v[180:181], v[152:153], v[112:113] op_sel_hi:[0,1]
	v_lshl_add_u64 v[154:155], s[96:97], 0, v[154:155]
	s_mov_b64 s[0:1], -1
	s_and_b64 vcc, exec, s[2:3]
	v_lshl_add_u64 v[154:155], v[66:67], 1, v[154:155]
	s_nop 0
	v_pk_mul_f32 v[158:159], v[158:159], v[230:231]
	v_pk_mul_f32 v[164:165], v[164:165], v[228:229]
	s_nop 0
	v_pk_mul_f32 v[160:161], v[178:179], v[234:235]
	v_pk_mul_f32 v[162:163], v[180:181], v[232:233]
	s_cbranch_vccz .LBB0_256
	v_cvt_pk_bf16_f32 v174, v164, v165
	v_cvt_pk_bf16_f32 v175, v158, v159
	v_cvt_pk_bf16_f32 v176, v162, v163
	v_cvt_pk_bf16_f32 v177, v160, v161
	global_store_dwordx4 v[154:155], v[174:177], off
	s_mov_b64 s[0:1], 0

.LBB0_258:
	s_nop 0
	s_nop 0
	s_nop 0
	v_mov_b32_e32 v153, v152
	v_mov_b32_e32 v162, v152
	v_mov_b32_e32 v163, v152
	v_pk_mul_f32 v[164:165], v[162:163], v[88:89]
	v_pk_mul_f32 v[178:179], v[152:153], v[90:91]
	v_pk_mul_f32 v[180:181], v[162:163], v[92:93]
	v_pk_mul_f32 v[208:209], v[152:153], v[94:95]
	s_mov_b64 s[0:1], -1
	s_and_b64 vcc, exec, s[2:3]
	s_nop 0
	v_pk_mul_f32 v[152:153], v[164:165], v[238:239]
	v_pk_mul_f32 v[162:163], v[178:179], v[236:237]
	s_nop 0
	v_pk_mul_f32 v[158:159], v[180:181], v[242:243]
	v_pk_mul_f32 v[160:161], v[208:209], v[240:241]
	s_cbranch_vccz .LBB0_260
	v_cvt_pk_bf16_f32 v174, v162, v163
	v_cvt_pk_bf16_f32 v175, v152, v153
	v_cvt_pk_bf16_f32 v176, v160, v161
	v_cvt_pk_bf16_f32 v177, v158, v159
	global_store_dwordx4 v[154:155], v[174:177], off offset:256
	s_mov_b64 s[0:1], 0

.LBB0_262:
	s_nop 0
	s_nop 0
	v_or_b32_e32 v154, 32, v76
	v_ashrrev_i32_e32 v155, 31, v154
	v_lshlrev_b64 v[152:153], 14, v[154:155]
	v_pk_mul_f32 v[156:157], v[150:151], v[110:111] op_sel_hi:[0,1]
	v_pk_mul_f32 v[162:163], v[150:151], v[108:109] op_sel_hi:[0,1]
	v_pk_mul_f32 v[164:165], v[150:151], v[106:107] op_sel_hi:[0,1]
	v_pk_mul_f32 v[178:179], v[150:151], v[104:105] op_sel_hi:[0,1]
	v_lshl_add_u64 v[152:153], s[96:97], 0, v[152:153]
	s_mov_b64 s[0:1], -1
	s_and_b64 vcc, exec, s[2:3]
	v_lshl_add_u64 v[152:153], v[66:67], 1, v[152:153]
	s_nop 0
	v_pk_mul_f32 v[156:157], v[156:157], v[230:231]
	v_pk_mul_f32 v[162:163], v[162:163], v[228:229]
	s_nop 0
	v_pk_mul_f32 v[158:159], v[164:165], v[234:235]
	v_pk_mul_f32 v[160:161], v[178:179], v[232:233]
	s_cbranch_vccz .LBB0_264
	v_cvt_pk_bf16_f32 v174, v162, v163
	v_cvt_pk_bf16_f32 v175, v156, v157
	v_cvt_pk_bf16_f32 v176, v160, v161
	v_cvt_pk_bf16_f32 v177, v158, v159
	global_store_dwordx4 v[152:153], v[174:177], off
	s_mov_b64 s[0:1], 0

.LBB0_266:
	s_nop 0
	s_nop 0
	s_nop 0
	v_mov_b32_e32 v151, v150
	v_mov_b32_e32 v160, v150
	v_mov_b32_e32 v161, v150
	v_pk_mul_f32 v[174:175], v[160:161], v[78:79]
	v_pk_mul_f32 v[176:177], v[150:151], v[80:81]
	v_pk_mul_f32 v[178:179], v[160:161], v[82:83]
	v_pk_mul_f32 v[180:181], v[150:151], v[84:85]
	s_mov_b64 s[0:1], -1
	s_and_b64 vcc, exec, s[2:3]
	s_nop 0
	v_pk_mul_f32 v[150:151], v[174:175], v[238:239]
	v_pk_mul_f32 v[160:161], v[176:177], v[236:237]
	s_nop 0
	v_pk_mul_f32 v[156:157], v[178:179], v[242:243]
	v_pk_mul_f32 v[158:159], v[180:181], v[240:241]
	s_cbranch_vccz .LBB0_268
	v_cvt_pk_bf16_f32 v162, v160, v161
	v_cvt_pk_bf16_f32 v163, v150, v151
	v_cvt_pk_bf16_f32 v164, v158, v159
	v_cvt_pk_bf16_f32 v165, v156, v157
	global_store_dwordx4 v[152:153], v[162:165], off offset:256
	s_mov_b64 s[0:1], 0

.LBB0_270:
	s_nop 0
	s_nop 0
	v_or_b32_e32 v152, 48, v76
	v_ashrrev_i32_e32 v153, 31, v152
	v_lshlrev_b64 v[150:151], 14, v[152:153]
	v_pk_mul_f32 v[154:155], v[148:149], v[102:103] op_sel_hi:[0,1]
	v_pk_mul_f32 v[160:161], v[148:149], v[100:101] op_sel_hi:[0,1]
	v_pk_mul_f32 v[174:175], v[148:149], v[98:99] op_sel_hi:[0,1]
	v_pk_mul_f32 v[176:177], v[148:149], v[96:97] op_sel_hi:[0,1]
	v_lshl_add_u64 v[150:151], s[96:97], 0, v[150:151]
	s_mov_b64 s[0:1], -1
	s_and_b64 vcc, exec, s[2:3]
	v_lshl_add_u64 v[150:151], v[66:67], 1, v[150:151]
	s_nop 0
	v_pk_mul_f32 v[154:155], v[154:155], v[230:231]
	v_pk_mul_f32 v[160:161], v[160:161], v[228:229]
	s_nop 0
	v_pk_mul_f32 v[156:157], v[174:175], v[234:235]
	v_pk_mul_f32 v[158:159], v[176:177], v[232:233]
	s_cbranch_vccz .LBB0_272
	v_cvt_pk_bf16_f32 v162, v160, v161
	v_cvt_pk_bf16_f32 v163, v154, v155
	v_cvt_pk_bf16_f32 v164, v158, v159
	v_cvt_pk_bf16_f32 v165, v156, v157
	global_store_dwordx4 v[150:151], v[162:165], off
	s_mov_b64 s[0:1], 0

.LBB0_274:
	s_nop 0
	s_nop 0
	s_nop 0
	v_mov_b32_e32 v149, v148
	v_mov_b32_e32 v158, v148
	v_mov_b32_e32 v159, v148
	v_pk_mul_f32 v[164:165], v[158:159], v[70:71]
	v_pk_mul_f32 v[174:175], v[148:149], v[68:69]
	v_pk_mul_f32 v[176:177], v[158:159], v[72:73]
	v_pk_mul_f32 v[178:179], v[148:149], v[74:75]
	s_mov_b64 s[0:1], -1
	s_and_b64 vcc, exec, s[2:3]
	s_nop 0
	v_pk_mul_f32 v[148:149], v[164:165], v[238:239]
	v_pk_mul_f32 v[158:159], v[174:175], v[236:237]
	s_nop 0
	v_pk_mul_f32 v[154:155], v[176:177], v[242:243]
	v_pk_mul_f32 v[156:157], v[178:179], v[240:241]
	s_cbranch_vccz .LBB0_276
	v_cvt_pk_bf16_f32 v160, v158, v159
	v_cvt_pk_bf16_f32 v161, v148, v149
	v_cvt_pk_bf16_f32 v162, v156, v157
	v_cvt_pk_bf16_f32 v163, v154, v155
	global_store_dwordx4 v[150:151], v[160:163], off offset:256
	s_mov_b64 s[0:1], 0

.LBB0_278:
	s_nop 0
	s_nop 0
	v_add_u32_e32 v150, 0x80, v76
	v_ashrrev_i32_e32 v151, 31, v150
	v_lshlrev_b64 v[148:149], 14, v[150:151]
	v_pk_mul_f32 v[152:153], v[146:147], v[62:63] op_sel_hi:[0,1]
	v_pk_mul_f32 v[158:159], v[146:147], v[60:61] op_sel_hi:[0,1]
	v_pk_mul_f32 v[164:165], v[146:147], v[58:59] op_sel_hi:[0,1]
	v_pk_mul_f32 v[174:175], v[146:147], v[64:65] op_sel_hi:[0,1]
	v_lshl_add_u64 v[148:149], s[96:97], 0, v[148:149]
	s_mov_b64 s[0:1], -1
	s_and_b64 vcc, exec, s[2:3]
	v_lshl_add_u64 v[148:149], v[66:67], 1, v[148:149]
	s_nop 0
	v_pk_mul_f32 v[152:153], v[152:153], v[230:231]
	v_pk_mul_f32 v[158:159], v[158:159], v[228:229]
	s_nop 0
	v_pk_mul_f32 v[154:155], v[164:165], v[234:235]
	v_pk_mul_f32 v[156:157], v[174:175], v[232:233]
	s_cbranch_vccz .LBB0_280
	v_cvt_pk_bf16_f32 v160, v158, v159
	v_cvt_pk_bf16_f32 v161, v152, v153
	v_cvt_pk_bf16_f32 v162, v156, v157
	v_cvt_pk_bf16_f32 v163, v154, v155
	global_store_dwordx4 v[148:149], v[160:163], off
	s_mov_b64 s[0:1], 0

.LBB0_282:
	s_nop 0
	s_nop 0
	s_nop 0
	v_mov_b32_e32 v147, v146
	v_mov_b32_e32 v156, v146
	v_mov_b32_e32 v157, v146
	v_pk_mul_f32 v[162:163], v[156:157], v[30:31]
	v_pk_mul_f32 v[164:165], v[146:147], v[28:29]
	v_pk_mul_f32 v[174:175], v[156:157], v[26:27]
	v_pk_mul_f32 v[176:177], v[146:147], v[24:25]
	s_mov_b64 s[0:1], -1
	s_and_b64 vcc, exec, s[2:3]
	s_nop 0
	v_pk_mul_f32 v[146:147], v[162:163], v[238:239]
	v_pk_mul_f32 v[156:157], v[164:165], v[236:237]
	s_nop 0
	v_pk_mul_f32 v[152:153], v[174:175], v[242:243]
	v_pk_mul_f32 v[154:155], v[176:177], v[240:241]
	s_cbranch_vccz .LBB0_284
	v_cvt_pk_bf16_f32 v158, v156, v157
	v_cvt_pk_bf16_f32 v159, v146, v147
	v_cvt_pk_bf16_f32 v160, v154, v155
	v_cvt_pk_bf16_f32 v161, v152, v153
	global_store_dwordx4 v[148:149], v[158:161], off offset:256
	s_mov_b64 s[0:1], 0

.LBB0_286:
	s_nop 0
	s_nop 0
	v_add_u32_e32 v148, 0x90, v76
	v_ashrrev_i32_e32 v149, 31, v148
	v_lshlrev_b64 v[146:147], 14, v[148:149]
	v_pk_mul_f32 v[150:151], v[144:145], v[54:55] op_sel_hi:[0,1]
	v_pk_mul_f32 v[156:157], v[144:145], v[52:53] op_sel_hi:[0,1]
	v_pk_mul_f32 v[162:163], v[144:145], v[50:51] op_sel_hi:[0,1]
	v_pk_mul_f32 v[164:165], v[144:145], v[48:49] op_sel_hi:[0,1]
	v_lshl_add_u64 v[146:147], s[96:97], 0, v[146:147]
	s_mov_b64 s[0:1], -1
	s_and_b64 vcc, exec, s[2:3]
	v_lshl_add_u64 v[146:147], v[66:67], 1, v[146:147]
	s_nop 0
	v_pk_mul_f32 v[150:151], v[150:151], v[230:231]
	v_pk_mul_f32 v[156:157], v[156:157], v[228:229]
	s_nop 0
	v_pk_mul_f32 v[152:153], v[162:163], v[234:235]
	v_pk_mul_f32 v[154:155], v[164:165], v[232:233]
	s_cbranch_vccz .LBB0_288
	v_cvt_pk_bf16_f32 v158, v156, v157
	v_cvt_pk_bf16_f32 v159, v150, v151
	v_cvt_pk_bf16_f32 v160, v154, v155
	v_cvt_pk_bf16_f32 v161, v152, v153
	global_store_dwordx4 v[146:147], v[158:161], off
	s_mov_b64 s[0:1], 0

.LBB0_290:
	s_nop 0
	s_nop 0
	s_nop 0
	v_mov_b32_e32 v145, v144
	v_mov_b32_e32 v154, v144
	v_mov_b32_e32 v155, v144
	v_pk_mul_f32 v[160:161], v[154:155], v[22:23]
	v_pk_mul_f32 v[162:163], v[144:145], v[20:21]
	v_pk_mul_f32 v[164:165], v[154:155], v[18:19]
	v_pk_mul_f32 v[174:175], v[144:145], v[16:17]
	s_mov_b64 s[0:1], -1
	s_and_b64 vcc, exec, s[2:3]
	s_nop 0
	v_pk_mul_f32 v[144:145], v[160:161], v[238:239]
	v_pk_mul_f32 v[154:155], v[162:163], v[236:237]
	s_nop 0
	v_pk_mul_f32 v[150:151], v[164:165], v[242:243]
	v_pk_mul_f32 v[152:153], v[174:175], v[240:241]
	s_cbranch_vccz .LBB0_292
	v_cvt_pk_bf16_f32 v156, v154, v155
	v_cvt_pk_bf16_f32 v157, v144, v145
	v_cvt_pk_bf16_f32 v158, v152, v153
	v_cvt_pk_bf16_f32 v159, v150, v151
	global_store_dwordx4 v[146:147], v[156:159], off offset:256
	s_mov_b64 s[0:1], 0

.LBB0_294:
	s_nop 0
	s_nop 0
	v_add_u32_e32 v146, 0xa0, v76
	v_ashrrev_i32_e32 v147, 31, v146
	v_lshlrev_b64 v[144:145], 14, v[146:147]
	v_pk_mul_f32 v[148:149], v[134:135], v[46:47] op_sel_hi:[0,1]
	v_pk_mul_f32 v[154:155], v[134:135], v[44:45] op_sel_hi:[0,1]
	v_pk_mul_f32 v[160:161], v[134:135], v[42:43] op_sel_hi:[0,1]
	v_pk_mul_f32 v[162:163], v[134:135], v[40:41] op_sel_hi:[0,1]
	v_lshl_add_u64 v[144:145], s[96:97], 0, v[144:145]
	s_mov_b64 s[0:1], -1
	s_and_b64 vcc, exec, s[2:3]
	v_lshl_add_u64 v[144:145], v[66:67], 1, v[144:145]
	s_nop 0
	v_pk_mul_f32 v[148:149], v[148:149], v[230:231]
	v_pk_mul_f32 v[154:155], v[154:155], v[228:229]
	s_nop 0
	v_pk_mul_f32 v[150:151], v[160:161], v[234:235]
	v_pk_mul_f32 v[152:153], v[162:163], v[232:233]
	s_cbranch_vccz .LBB0_296
	v_cvt_pk_bf16_f32 v156, v154, v155
	v_cvt_pk_bf16_f32 v157, v148, v149
	v_cvt_pk_bf16_f32 v158, v152, v153
	v_cvt_pk_bf16_f32 v159, v150, v151
	global_store_dwordx4 v[144:145], v[156:159], off
	s_mov_b64 s[0:1], 0

.LBB0_298:
	s_nop 0
	s_nop 0
	s_nop 0
	v_mov_b32_e32 v135, v134
	v_mov_b32_e32 v152, v134
	v_mov_b32_e32 v153, v134
	v_pk_mul_f32 v[158:159], v[152:153], v[14:15]
	v_pk_mul_f32 v[160:161], v[134:135], v[12:13]
	v_pk_mul_f32 v[162:163], v[152:153], v[10:11]
	v_pk_mul_f32 v[164:165], v[134:135], v[8:9]
	s_mov_b64 s[0:1], -1
	s_and_b64 vcc, exec, s[2:3]
	s_nop 0
	v_pk_mul_f32 v[134:135], v[158:159], v[238:239]
	v_pk_mul_f32 v[152:153], v[160:161], v[236:237]
	s_nop 0
	v_pk_mul_f32 v[148:149], v[162:163], v[242:243]
	v_pk_mul_f32 v[150:151], v[164:165], v[240:241]
	s_cbranch_vccz .LBB0_300
	v_cvt_pk_bf16_f32 v154, v152, v153
	v_cvt_pk_bf16_f32 v155, v134, v135
	v_cvt_pk_bf16_f32 v156, v150, v151
	v_cvt_pk_bf16_f32 v157, v148, v149
	global_store_dwordx4 v[144:145], v[154:157], off offset:256
	s_mov_b64 s[0:1], 0

.LBB0_302:
	s_nop 0
	s_nop 0
	s_nop 0
	v_add_u32_e32 v86, 0xb0, v76
	v_ashrrev_i32_e32 v87, 31, v86
	v_lshlrev_b64 v[76:77], 14, v[86:87]
	v_pk_mul_f32 v[134:135], v[56:57], v[38:39] op_sel_hi:[0,1]
	v_pk_mul_f32 v[148:149], v[56:57], v[36:37] op_sel_hi:[0,1]
	v_pk_mul_f32 v[154:155], v[56:57], v[34:35] op_sel_hi:[0,1]
	v_pk_mul_f32 v[156:157], v[56:57], v[32:33] op_sel_hi:[0,1]
	v_lshl_add_u64 v[76:77], s[96:97], 0, v[76:77]
	s_mov_b64 s[0:1], -1
	s_and_b64 vcc, exec, s[2:3]
	v_lshl_add_u64 v[76:77], v[66:67], 1, v[76:77]
	s_nop 0
	v_pk_mul_f32 v[134:135], v[134:135], v[230:231]
	v_pk_mul_f32 v[148:149], v[148:149], v[228:229]
	s_nop 0
	v_pk_mul_f32 v[144:145], v[154:155], v[234:235]
	v_pk_mul_f32 v[146:147], v[156:157], v[232:233]
	s_cbranch_vccz .LBB0_304
	v_cvt_pk_bf16_f32 v150, v148, v149
	v_cvt_pk_bf16_f32 v151, v134, v135
	v_cvt_pk_bf16_f32 v152, v146, v147
	v_cvt_pk_bf16_f32 v153, v144, v145
	global_store_dwordx4 v[76:77], v[150:153], off
	s_mov_b64 s[0:1], 0

.LBB0_306:
	s_nop 0
	s_nop 0
	v_mov_b32_e32 v57, v56
	v_mov_b32_e32 v86, v56
	v_mov_b32_e32 v87, v56
	v_pk_mul_f32 v[120:121], v[86:87], v[6:7]
	v_pk_mul_f32 v[134:135], v[56:57], v[4:5]
	v_pk_mul_f32 v[86:87], v[86:87], v[2:3]
	v_pk_mul_f32 v[152:153], v[56:57], v[0:1]
	s_mov_b64 s[0:1], -1
	s_and_b64 vcc, exec, s[2:3]
	s_nop 0
	v_pk_mul_f32 v[56:57], v[120:121], v[238:239]
	v_pk_mul_f32 v[134:135], v[134:135], v[236:237]
	s_nop 0
	v_pk_mul_f32 v[86:87], v[86:87], v[242:243]
	v_pk_mul_f32 v[120:121], v[152:153], v[240:241]
	s_cbranch_vccz .LBB0_308
	v_cvt_pk_bf16_f32 v144, v134, v135
	v_cvt_pk_bf16_f32 v145, v56, v57
	v_cvt_pk_bf16_f32 v146, v120, v121
	v_cvt_pk_bf16_f32 v147, v86, v87
	global_store_dwordx4 v[76:77], v[144:147], off offset:256
	s_mov_b64 s[0:1], 0

.LBB0_328:
	v_readlane_b32 s14, v253, 26
	v_ashrrev_i32_e32 v57, 31, v56
	v_readlane_b32 s15, v253, 27
	s_lshl_b32 s10, s10, 8
	s_ashr_i32 s11, s10, 31
	v_lshl_add_u64 v[66:67], v[56:57], 2, s[14:15]
	global_load_dword v163, v[66:67], off
	v_lshl_add_u64 v[66:67], s[10:11], 2, v[130:131]
	global_load_dwordx4 v[228:231], v[66:67], off offset:16
	global_load_dwordx4 v[232:235], v[66:67], off
	s_add_i32 s20, s10, 0xfffff000
	v_lshlrev_b64 v[160:161], 13, v[148:149]
	s_ashr_i32 s21, s20, 31
	s_mov_b64 s[22:23], -1
	s_and_b64 vcc, exec, s[0:1]
	s_waitcnt vmcnt(0)
	v_pk_mul_f32 v[150:151], v[232:233], v[138:139]
	v_lshl_add_u64 v[138:139], s[66:67], 0, v[160:161]
	v_pk_mul_f32 v[154:155], v[234:235], v[136:137]
	v_pk_mul_f32 v[152:153], v[230:231], v[140:141]
	v_pk_mul_f32 v[140:141], v[228:229], v[142:143]
	v_lshl_add_u64 v[136:137], s[20:21], 1, v[138:139]
	s_cbranch_vccz .LBB0_330
	v_lshl_add_u64 v[158:159], s[20:21], 1, v[138:139]
	s_mov_b64 s[22:23], 0
	v_mov_b32_e32 v161, v153
	v_mov_b32_e32 v160, v152
	v_mov_b32_e32 v157, v155
	v_mov_b32_e32 v156, v154

.LBB0_336:
	global_load_dwordx4 v[236:239], v[66:67], off offset:512
	s_nop 0
	global_load_dwordx4 v[240:243], v[66:67], off offset:528
	v_cndmask_b32_e64 v148, 0, 1, s[0:1]
	v_cmp_ne_u32_e64 s[36:37], 1, v148
	s_andn2_b64 vcc, exec, s[0:1]
	s_mov_b64 s[0:1], -1
	s_waitcnt vmcnt(1)
	v_pk_mul_f32 v[148:149], v[238:239], v[122:123]
	v_pk_mul_f32 v[122:123], v[236:237], v[124:125]
	s_waitcnt vmcnt(0)
	v_pk_mul_f32 v[126:127], v[242:243], v[126:127]
	v_pk_mul_f32 v[124:125], v[240:241], v[132:133]
	s_cbranch_vccnz .LBB0_338
	s_mov_b64 s[0:1], 0

.LBB0_344:
	s_nop 0
	s_nop 0
	s_nop 0
	v_lshlrev_b64 v[126:127], 13, v[146:147]
	v_lshl_add_u64 v[136:137], s[66:67], 0, v[126:127]
	s_mov_b64 s[0:1], -1
	s_and_b64 vcc, exec, s[36:37]
	s_nop 0
	v_pk_mul_f32 v[126:127], v[234:235], v[118:119]
	v_pk_mul_f32 v[116:117], v[232:233], v[116:117]
	s_nop 0
	v_pk_mul_f32 v[124:125], v[230:231], v[114:115]
	v_pk_mul_f32 v[122:123], v[228:229], v[112:113]
	v_lshl_add_u64 v[112:113], s[20:21], 1, v[136:137]
	s_cbranch_vccnz .LBB0_346
	v_lshl_add_u64 v[132:133], s[20:21], 1, v[136:137]
	s_mov_b64 s[0:1], 0

.LBB0_352:
	s_nop 0
	s_nop 0
	s_and_b64 vcc, exec, s[36:37]
	s_mov_b64 s[0:1], -1
	s_nop 0
	v_pk_mul_f32 v[122:123], v[238:239], v[88:89]
	v_pk_mul_f32 v[88:89], v[236:237], v[90:91]
	s_nop 0
	v_pk_mul_f32 v[92:93], v[242:243], v[92:93]
	v_pk_mul_f32 v[90:91], v[240:241], v[94:95]
	s_cbranch_vccnz .LBB0_354
	s_mov_b64 s[0:1], 0

.LBB0_360:
	s_nop 0
	s_nop 0
	s_nop 0
	v_lshlrev_b64 v[88:89], 13, v[144:145]
	v_lshl_add_u64 v[90:91], s[66:67], 0, v[88:89]
	s_mov_b64 s[0:1], -1
	s_and_b64 vcc, exec, s[36:37]
	v_lshl_add_u64 v[88:89], s[20:21], 1, v[90:91]
	s_nop 0
	v_pk_mul_f32 v[110:111], v[234:235], v[110:111]
	v_pk_mul_f32 v[92:93], v[232:233], v[108:109]
	s_nop 0
	v_pk_mul_f32 v[106:107], v[230:231], v[106:107]
	v_pk_mul_f32 v[104:105], v[228:229], v[104:105]
	s_cbranch_vccnz .LBB0_362
	v_lshl_add_u64 v[108:109], s[20:21], 1, v[90:91]
	s_mov_b64 s[0:1], 0

.LBB0_368:
	s_nop 0
	s_nop 0
	s_nop 0
	s_and_b64 vcc, exec, s[36:37]
	s_mov_b64 s[0:1], -1
	s_nop 0
	v_pk_mul_f32 v[104:105], v[238:239], v[78:79]
	v_pk_mul_f32 v[78:79], v[236:237], v[80:81]
	s_nop 0
	v_pk_mul_f32 v[82:83], v[242:243], v[82:83]
	v_pk_mul_f32 v[80:81], v[240:241], v[84:85]
	s_cbranch_vccnz .LBB0_370
	s_mov_b64 s[0:1], 0

.LBB0_376:
	s_nop 0
	s_nop 0
	s_nop 0
	v_lshlrev_b64 v[78:79], 13, v[134:135]
	v_lshl_add_u64 v[80:81], s[66:67], 0, v[78:79]
	s_mov_b64 s[0:1], -1
	s_and_b64 vcc, exec, s[36:37]
	v_lshl_add_u64 v[78:79], s[20:21], 1, v[80:81]
	s_nop 0
	v_pk_mul_f32 v[92:93], v[234:235], v[102:103]
	v_pk_mul_f32 v[82:83], v[232:233], v[100:101]
	s_nop 0
	v_pk_mul_f32 v[90:91], v[230:231], v[98:99]
	v_pk_mul_f32 v[88:89], v[228:229], v[96:97]
	s_cbranch_vccnz .LBB0_378
	v_lshl_add_u64 v[94:95], s[20:21], 1, v[80:81]
	s_mov_b64 s[0:1], 0

.LBB0_384:
	s_nop 0
	s_nop 0
	s_nop 0
	s_and_b64 vcc, exec, s[36:37]
	s_mov_b64 s[0:1], -1
	s_nop 0
	v_pk_mul_f32 v[88:89], v[238:239], v[70:71]
	v_pk_mul_f32 v[68:69], v[236:237], v[68:69]
	s_nop 0
	v_pk_mul_f32 v[72:73], v[242:243], v[72:73]
	v_pk_mul_f32 v[70:71], v[240:241], v[74:75]
	s_cbranch_vccnz .LBB0_386
	s_mov_b64 s[0:1], 0

.LBB0_392:
	s_nop 0
	s_nop 0
	s_nop 0
	v_lshlrev_b64 v[72:73], 13, v[120:121]
	v_lshl_add_u64 v[78:79], s[66:67], 0, v[72:73]
	s_mov_b64 s[0:1], -1
	s_and_b64 vcc, exec, s[36:37]
	s_nop 0
	v_pk_mul_f32 v[72:73], v[234:235], v[62:63]
	v_pk_mul_f32 v[62:63], v[232:233], v[60:61]
	s_nop 0
	v_pk_mul_f32 v[70:71], v[230:231], v[58:59]
	v_pk_mul_f32 v[68:69], v[228:229], v[64:65]
	v_lshl_add_u64 v[58:59], s[20:21], 1, v[78:79]
	s_cbranch_vccnz .LBB0_394
	v_lshl_add_u64 v[74:75], s[20:21], 1, v[78:79]
	s_mov_b64 s[0:1], 0

.LBB0_400:
	s_nop 0
	s_nop 0
	s_nop 0
	s_and_b64 vcc, exec, s[36:37]
	s_mov_b64 s[0:1], -1
	s_nop 0
	v_pk_mul_f32 v[30:31], v[238:239], v[30:31]
	v_pk_mul_f32 v[28:29], v[236:237], v[28:29]
	s_nop 0
	v_pk_mul_f32 v[26:27], v[242:243], v[26:27]
	v_pk_mul_f32 v[24:25], v[240:241], v[24:25]
	s_cbranch_vccnz .LBB0_402
	s_mov_b64 s[0:1], 0

.LBB0_408:
	s_nop 0
	s_nop 0
	s_nop 0
	v_lshlrev_b64 v[24:25], 13, v[86:87]
	v_lshl_add_u64 v[26:27], s[66:67], 0, v[24:25]
	s_mov_b64 s[0:1], -1
	s_and_b64 vcc, exec, s[36:37]
	v_lshl_add_u64 v[24:25], s[20:21], 1, v[26:27]
	s_nop 0
	v_pk_mul_f32 v[54:55], v[234:235], v[54:55]
	v_pk_mul_f32 v[28:29], v[232:233], v[52:53]
	s_nop 0
	v_pk_mul_f32 v[50:51], v[230:231], v[50:51]
	v_pk_mul_f32 v[48:49], v[228:229], v[48:49]
	s_cbranch_vccnz .LBB0_410
	v_lshl_add_u64 v[52:53], s[20:21], 1, v[26:27]
	s_mov_b64 s[0:1], 0

.LBB0_416:
	s_nop 0
	s_nop 0
	s_nop 0
	s_and_b64 vcc, exec, s[36:37]
	s_mov_b64 s[0:1], -1
	s_nop 0
	v_pk_mul_f32 v[22:23], v[238:239], v[22:23]
	v_pk_mul_f32 v[20:21], v[236:237], v[20:21]
	s_nop 0
	v_pk_mul_f32 v[18:19], v[242:243], v[18:19]
	v_pk_mul_f32 v[16:17], v[240:241], v[16:17]
	s_cbranch_vccnz .LBB0_418
	s_mov_b64 s[0:1], 0

.LBB0_424:
	s_nop 0
	s_nop 0
	s_nop 0
	v_lshlrev_b64 v[16:17], 13, v[76:77]
	v_lshl_add_u64 v[18:19], s[66:67], 0, v[16:17]
	s_mov_b64 s[0:1], -1
	s_and_b64 vcc, exec, s[36:37]
	v_lshl_add_u64 v[16:17], s[20:21], 1, v[18:19]
	s_nop 0
	v_pk_mul_f32 v[28:29], v[234:235], v[46:47]
	v_pk_mul_f32 v[20:21], v[232:233], v[44:45]
	s_nop 0
	v_pk_mul_f32 v[26:27], v[230:231], v[42:43]
	v_pk_mul_f32 v[24:25], v[228:229], v[40:41]
	s_cbranch_vccnz .LBB0_426
	v_lshl_add_u64 v[30:31], s[20:21], 1, v[18:19]
	s_mov_b64 s[0:1], 0

.LBB0_432:
	s_nop 0
	s_nop 0
	s_nop 0
	s_and_b64 vcc, exec, s[36:37]
	s_mov_b64 s[0:1], -1
	s_nop 0
	v_pk_mul_f32 v[14:15], v[238:239], v[14:15]
	v_pk_mul_f32 v[12:13], v[236:237], v[12:13]
	s_nop 0
	v_pk_mul_f32 v[10:11], v[242:243], v[10:11]
	v_pk_mul_f32 v[8:9], v[240:241], v[8:9]
	s_cbranch_vccnz .LBB0_434
	s_mov_b64 s[0:1], 0

.LBB0_440:
	s_nop 0
	s_nop 0
	s_nop 0
	v_lshlrev_b64 v[8:9], 13, v[56:57]
	v_lshl_add_u64 v[10:11], s[66:67], 0, v[8:9]
	s_mov_b64 s[0:1], -1
	s_and_b64 vcc, exec, s[36:37]
	v_lshl_add_u64 v[8:9], s[20:21], 1, v[10:11]
	s_nop 0
	v_pk_mul_f32 v[20:21], v[234:235], v[38:39]
	v_pk_mul_f32 v[12:13], v[232:233], v[36:37]
	s_nop 0
	v_pk_mul_f32 v[18:19], v[230:231], v[34:35]
	v_pk_mul_f32 v[16:17], v[228:229], v[32:33]
	s_cbranch_vccnz .LBB0_442
	v_lshl_add_u64 v[22:23], s[20:21], 1, v[10:11]
	s_mov_b64 s[0:1], 0

.LBB0_448:
	s_nop 0
	s_nop 0
	s_nop 0
	s_and_b64 vcc, exec, s[36:37]
	s_mov_b64 s[0:1], -1
	s_nop 0
	v_pk_mul_f32 v[6:7], v[238:239], v[6:7]
	v_pk_mul_f32 v[4:5], v[236:237], v[4:5]
	s_nop 0
	v_pk_mul_f32 v[2:3], v[242:243], v[2:3]
	v_pk_mul_f32 v[0:1], v[240:241], v[0:1]
	s_cbranch_vccnz .LBB0_450
	s_mov_b64 s[0:1], 0
